# as previous plus the vmcnt(0) before the last store of the P1 fp8 projection epilogue (all waves) replaced by s_nop: it only waited for store acknowledgements
# baseline (speedup 1.0000x reference)
.LBB0_455:
	s_andn2_b64 vcc, exec, s[72:73]
	s_mov_b64 s[4:5], -1
	s_nop 0
	v_cvt_pk_bf16_f32 v0, v20, v21
	v_cvt_pk_bf16_f32 v1, v18, v19
	v_cvt_pk_bf16_f32 v2, v24, v25
	v_cvt_pk_bf16_f32 v3, v22, v23
	global_store_dwordx4 v[16:17], v[0:3], off offset:256
	s_cbranch_vccnz .LBB0_342
	s_andn2_b64 vcc, exec, s[40:41]
	s_cbranch_vccnz .LBB0_341
	s_barrier
	s_branch .LBB0_341
